# in-proj and MoE-down GEMMs: first K double-step of each tile peeled with C=0 for the first MFMA of every accumulator; the 128-instruction accumulator zeroing at each tile top removed
# speedup vs baseline: 1.0040x; 1.0040x over previous
; #define PG8_SETA(d0, d1, u) do { d0.x = PG8_OFFA(u, Rr[0], 0); d0.y = PG8_OFFA(u, Rr[1], 1); d1.x = PG8_OFFA(u, HALF + Rr[0], 0); d1.y = PG8_OFFA(u, HALF + Rr[1], 1); } while (0)
; #define PG8_STAGE_A(bufoff, soff, voff) do { _Pragma("unroll") for (int _i = 0; _i < 2; ++_i) \
;         __builtin_amdgcn_raw_ptr_buffer_load_lds(rsA, (LAS void*)(lds + (bufoff) + ldsw + _i * 8192), 16, (voff)[_i], (soff), 0, 0); } while (0)
; #define PG8_STAGE_B(bufoff, soff) do { _Pragma("unroll") for (int _i = 0; _i < 2; ++_i) \
;         __builtin_amdgcn_raw_ptr_buffer_load_lds(rsB, (LAS void*)(lds + (bufoff) + ldsw + _i * 8192), 16, voffB[_i], (soff), 0, 0); } while (0)
; #define PG8_LDA(dst, b, h) do { _Pragma("unroll") for (int m = 0; m < 4; ++m) dst[m] = PG8_LD8(lds + PG8_SA(b, h) + aoff + m * 2048); } while (0)
; #define PG8_WAIT_V(n) asm volatile("s_waitcnt vmcnt(" #n ")" ::: "memory")
; template <class Epi, class Sched, bool GATHER, bool ALIGN_EPI, bool SP2, bool FP8>
; __device__ __forceinline__ void gemm_phase(LAS unsigned char* lds, const Gemm g, const Sched& S, const Epi& E) {
;     ...
;     for (;;) {
;         const bool has_next = S.next(ui + 1, nxt);
;         const int nA = has_next ? (GATHER ? 0 : nxt.pm * tstep) : cA, nB = has_next ? nxt.pn * tstep : cB;
;         u32x2 nvA0 = vA0, nvA1 = vA1;
;         if constexpr (GATHER) { if (has_next) PG8_SETA(nvA0, nvA1, nxt); }
;         for (int t = 0; t < nt; t += 2) {
;             const bool last = (t == nt - 2);
;             if (last) pre = E.prefetch(cur, wr, wc, fr, fq);
;             const int a1 = cA + (t + 1) * kstep;
;             const int a2 = last ? nA : cA + (t + 2) * kstep, b2 = last ? nB : cB + (t + 2) * kstep;
;             const int a3 = a2 + kstep, b3 = b2 + kstep;
;             const u32x2 va20 = (GATHER && last) ? nvA0 : vA0, va21 = (GATHER && last) ? nvA1 : vA1;
;             if constexpr (SP2) {
;             PG8_LDB(B0, 0, 0); PG8_LDB(B1, 0, 1); PG8_SCHED; PG8_LDA(At, 0, 0); PG8_STAGE_A(PG8_SA(1, 1), a1, vA1);
;             PG8_WAIT_V(8); PG8_WAIT_L(0); PG8_BAR; PG8_MMA(0, 0, At, B0); PG8_MMA(0, 1, At, B1); PG8_BAR; PG8_SCHED;
;             PG8_LDA(At, 0, 1); PG8_STAGE_B(PG8_SB(0, 0), b2); PG8_STAGE_B(PG8_SB(0, 1), b2 + hstep); PG8_STAGE_A(PG8_SA(0, 0), a2, va20);
;             PG8_WAIT_V(8); PG8_WAIT_L(0); PG8_BAR; PG8_MMA(1, 0, At, B0); PG8_MMA(1, 1, At, B1); PG8_BAR; PG8_SCHED;
.LBB0_190:
	v_cmp_lt_i64_e32 vcc, s[10:11], v[166:167]
	s_lshl_b32 s33, s44, 20
	s_and_b64 s[10:11], vcc, exec
	v_lshl_add_u32 v2, s47, 8, v185
	s_cselect_b32 s48, s33, s50
	s_lshl_b32 s45, s43, 20
	v_ashrrev_i32_e32 v3, 31, v2
	s_and_b64 s[10:11], vcc, exec
	v_lshl_add_u64 v[178:179], v[2:3], 2, s[16:17]
	s_cselect_b32 s49, s45, s51
	s_addk_i32 s50, 0x80
	s_addk_i32 s51, 0x100
	s_mov_b32 s52, -2
	s_waitcnt vmcnt(32)
	s_waitcnt vmcnt(31)
	s_waitcnt vmcnt(30)
	s_waitcnt vmcnt(29)
	s_waitcnt vmcnt(28)
	s_waitcnt vmcnt(27)
	s_waitcnt vmcnt(25)
	s_waitcnt vmcnt(24)
	s_waitcnt vmcnt(23)
	s_waitcnt vmcnt(22)
	s_mov_b64 s[10:11], 0
	v_add_u32_e32 v130, 0x10000, v186
	v_add_u32_e32 v131, 0x14000, v186
	ds_read_b128 v[158:161], v130
	ds_read_b128 v[154:157], v130 offset:1024
	ds_read_b128 v[150:153], v130 offset:2048
	ds_read_b128 v[146:149], v130 offset:3072
	ds_read_b128 v[142:145], v131
	ds_read_b128 v[138:141], v131 offset:1024
	ds_read_b128 v[134:137], v131 offset:2048
	ds_read_b128 v[130:133], v131 offset:3072
	s_add_i32 s53, s50, 0x80
	s_and_b64 s[56:57], s[10:11], exec
	s_cselect_b32 s57, s48, s53
	s_or_b32 s53, s57, 0x80
	s_and_b64 s[10:11], s[10:11], exec
	s_cselect_b32 s56, s49, s51
	s_mov_b32 m0, s39
	ds_read_b128 v[188:191], v187
	ds_read_b128 v[192:195], v187 offset:1024
	ds_read_b128 v[196:199], v187 offset:2048
	ds_read_b128 v[200:203], v187 offset:3072
	ds_read_b128 v[204:207], v187 offset:4096
	ds_read_b128 v[208:211], v187 offset:5120
	ds_read_b128 v[212:215], v187 offset:6144
	ds_read_b128 v[216:219], v187 offset:7168
	buffer_load_dwordx4 v183, s[4:7], s50 offen lds
	s_mov_b32 m0, s40
	s_nop 0
	buffer_load_dwordx4 v184, s[4:7], s50 offen lds
	s_waitcnt vmcnt(8)
	s_waitcnt lgkmcnt(0)
	s_barrier
	s_setprio 1
	s_waitcnt lgkmcnt(7)
	v_mfma_f32_16x16x32_bf16 v[126:129], v[158:161], v[188:191], 0
	s_waitcnt lgkmcnt(6)
	v_mfma_f32_16x16x32_bf16 v[126:129], v[154:157], v[192:195], v[126:129]
	v_mfma_f32_16x16x32_bf16 v[122:125], v[150:153], v[188:191], 0
	s_nop 0
	v_mfma_f32_16x16x32_bf16 v[122:125], v[146:149], v[192:195], v[122:125]
	s_waitcnt lgkmcnt(5)
	v_mfma_f32_16x16x32_bf16 v[118:121], v[158:161], v[196:199], 0
	s_waitcnt lgkmcnt(4)
	v_mfma_f32_16x16x32_bf16 v[118:121], v[154:157], v[200:203], v[118:121]
	v_mfma_f32_16x16x32_bf16 v[110:113], v[150:153], v[196:199], 0
	s_nop 0
	v_mfma_f32_16x16x32_bf16 v[110:113], v[146:149], v[200:203], v[110:113]
	s_waitcnt lgkmcnt(3)
	v_mfma_f32_16x16x32_bf16 v[102:105], v[158:161], v[204:207], 0
	s_waitcnt lgkmcnt(2)
	v_mfma_f32_16x16x32_bf16 v[102:105], v[154:157], v[208:211], v[102:105]
	v_mfma_f32_16x16x32_bf16 v[94:97], v[150:153], v[204:207], 0
	s_nop 0
	v_mfma_f32_16x16x32_bf16 v[94:97], v[146:149], v[208:211], v[94:97]
	s_waitcnt lgkmcnt(1)
	v_mfma_f32_16x16x32_bf16 v[86:89], v[158:161], v[212:215], 0
	s_waitcnt lgkmcnt(0)
	v_mfma_f32_16x16x32_bf16 v[86:89], v[154:157], v[216:219], v[86:89]
	v_mfma_f32_16x16x32_bf16 v[78:81], v[150:153], v[212:215], 0
	s_nop 0
	v_mfma_f32_16x16x32_bf16 v[78:81], v[146:149], v[216:219], v[78:81]
	s_setprio 0
	s_setprio 1
	v_mfma_f32_16x16x32_bf16 v[114:117], v[142:145], v[188:191], 0
	s_nop 0
	v_mfma_f32_16x16x32_bf16 v[114:117], v[138:141], v[192:195], v[114:117]
	v_mfma_f32_16x16x32_bf16 v[106:109], v[134:137], v[188:191], 0
	s_nop 0
	v_mfma_f32_16x16x32_bf16 v[106:109], v[130:133], v[192:195], v[106:109]
	v_mfma_f32_16x16x32_bf16 v[98:101], v[142:145], v[196:199], 0
	s_nop 0
	v_mfma_f32_16x16x32_bf16 v[98:101], v[138:141], v[200:203], v[98:101]
	v_mfma_f32_16x16x32_bf16 v[90:93], v[134:137], v[196:199], 0
	s_nop 0
	v_mfma_f32_16x16x32_bf16 v[90:93], v[130:133], v[200:203], v[90:93]
	v_mfma_f32_16x16x32_bf16 v[82:85], v[142:145], v[204:207], 0
	s_nop 0
	v_mfma_f32_16x16x32_bf16 v[82:85], v[138:141], v[208:211], v[82:85]
	v_mfma_f32_16x16x32_bf16 v[74:77], v[134:137], v[204:207], 0
	s_nop 0
	v_mfma_f32_16x16x32_bf16 v[74:77], v[130:133], v[208:211], v[74:77]
	v_mfma_f32_16x16x32_bf16 v[70:73], v[142:145], v[212:215], 0
	s_nop 0
	v_mfma_f32_16x16x32_bf16 v[70:73], v[138:141], v[216:219], v[70:73]
	v_mfma_f32_16x16x32_bf16 v[66:69], v[134:137], v[212:215], 0
	s_nop 0
	v_mfma_f32_16x16x32_bf16 v[66:69], v[130:133], v[216:219], v[66:69]
	s_setprio 0
	s_barrier
	s_mov_b32 m0, s23
	s_mov_b32 s10, s6
	s_mov_b32 s11, s7
	ds_read_b128 v[188:191], v187 offset:16384
	ds_read_b128 v[192:195], v187 offset:17408
	ds_read_b128 v[196:199], v187 offset:18432
	ds_read_b128 v[200:203], v187 offset:19456
	ds_read_b128 v[204:207], v187 offset:20480
	ds_read_b128 v[208:211], v187 offset:21504
	ds_read_b128 v[212:215], v187 offset:22528
	ds_read_b128 v[216:219], v187 offset:23552
	buffer_load_dwordx4 v165, s[8:11], s56 offen lds
	s_mov_b32 m0, s24
	s_add_i32 s58, s56, 0x80000
	buffer_load_dwordx4 v180, s[8:11], s56 offen lds
	s_mov_b32 m0, s25
	s_nop 0
	buffer_load_dwordx4 v165, s[8:11], s58 offen lds
	s_mov_b32 m0, s26
	s_nop 0
	buffer_load_dwordx4 v180, s[8:11], s58 offen lds
	s_mov_b32 m0, s22
	s_nop 0
	buffer_load_dwordx4 v181, s[4:7], s57 offen lds
	s_mov_b32 m0, s27
	s_nop 0
	buffer_load_dwordx4 v182, s[4:7], s57 offen lds
	s_waitcnt vmcnt(8)
	s_waitcnt lgkmcnt(0)
	s_barrier
; #define PG8_STAGE_A(bufoff, soff, voff) do { _Pragma("unroll") for (int _i = 0; _i < 2; ++_i) \
;         __builtin_amdgcn_raw_ptr_buffer_load_lds(rsA, (LAS void*)(lds + (bufoff) + ldsw + _i * 8192), 16, (voff)[_i], (soff), 0, 0); } while (0)
; #define PG8_LDA(dst, b, h) do { _Pragma("unroll") for (int m = 0; m < 4; ++m) dst[m] = PG8_LD8(lds + PG8_SA(b, h) + aoff + m * 2048); } while (0)
; #define PG8_LDB(dst, b, h) do { _Pragma("unroll") for (int n = 0; n < 2; ++n) dst[n] = PG8_LD8(lds + PG8_SB(b, h) + boff + n * 2048); } while (0)
; #define PG8_WAIT_V(n) asm volatile("s_waitcnt vmcnt(" #n ")" ::: "memory")
; #define PG8_WAIT_L(n) asm volatile("s_waitcnt lgkmcnt(" #n ")" ::: "memory")
; #define PG8_BAR __builtin_amdgcn_s_barrier()
; #define PG8_SCHED __builtin_amdgcn_sched_barrier(0)
; template <class Epi, class Sched, bool GATHER, bool ALIGN_EPI, bool SP2, bool FP8>
; __device__ __forceinline__ void gemm_phase(LAS unsigned char* lds, const Gemm g, const Sched& S, const Epi& E) {
;     ...
;             PG8_WAIT_V(8); PG8_WAIT_L(0); PG8_BAR; PG8_MMA(1, 0, At, B0); PG8_MMA(1, 1, At, B1); PG8_BAR; PG8_SCHED;
;             PG8_LDB(B0, 1, 0); PG8_LDB(B1, 1, 1); PG8_SCHED; PG8_LDA(At, 1, 0); PG8_STAGE_A(PG8_SA(0, 1), a2, va21);
;             PG8_WAIT_V(8); PG8_WAIT_L(0); PG8_BAR; PG8_MMA(0, 0, At, B0); PG8_MMA(0, 1, At, B1); PG8_BAR; PG8_SCHED;
	s_setprio 1
	s_waitcnt lgkmcnt(7)
	v_mfma_f32_16x16x32_bf16 v[62:65], v[158:161], v[188:191], 0
	s_waitcnt lgkmcnt(6)
	v_mfma_f32_16x16x32_bf16 v[62:65], v[154:157], v[192:195], v[62:65]
	v_mfma_f32_16x16x32_bf16 v[58:61], v[150:153], v[188:191], 0
	s_nop 0
	v_mfma_f32_16x16x32_bf16 v[58:61], v[146:149], v[192:195], v[58:61]
	s_waitcnt lgkmcnt(5)
	v_mfma_f32_16x16x32_bf16 v[54:57], v[158:161], v[196:199], 0
	s_waitcnt lgkmcnt(4)
	v_mfma_f32_16x16x32_bf16 v[54:57], v[154:157], v[200:203], v[54:57]
	v_mfma_f32_16x16x32_bf16 v[46:49], v[150:153], v[196:199], 0
	s_nop 0
	v_mfma_f32_16x16x32_bf16 v[46:49], v[146:149], v[200:203], v[46:49]
	s_waitcnt lgkmcnt(3)
	v_mfma_f32_16x16x32_bf16 v[38:41], v[158:161], v[204:207], 0
	s_waitcnt lgkmcnt(2)
	v_mfma_f32_16x16x32_bf16 v[38:41], v[154:157], v[208:211], v[38:41]
	v_mfma_f32_16x16x32_bf16 v[30:33], v[150:153], v[204:207], 0
	s_nop 0
	v_mfma_f32_16x16x32_bf16 v[30:33], v[146:149], v[208:211], v[30:33]
	s_waitcnt lgkmcnt(1)
	v_mfma_f32_16x16x32_bf16 v[22:25], v[158:161], v[212:215], 0
	s_waitcnt lgkmcnt(0)
	v_mfma_f32_16x16x32_bf16 v[22:25], v[154:157], v[216:219], v[22:25]
	v_mfma_f32_16x16x32_bf16 v[14:17], v[150:153], v[212:215], 0
	s_nop 0
	v_mfma_f32_16x16x32_bf16 v[14:17], v[146:149], v[216:219], v[14:17]
	s_setprio 0
	s_setprio 1
	v_mfma_f32_16x16x32_bf16 v[50:53], v[142:145], v[188:191], 0
	s_nop 0
	v_mfma_f32_16x16x32_bf16 v[50:53], v[138:141], v[192:195], v[50:53]
	v_mfma_f32_16x16x32_bf16 v[42:45], v[134:137], v[188:191], 0
	s_nop 0
	v_mfma_f32_16x16x32_bf16 v[42:45], v[130:133], v[192:195], v[42:45]
	v_mfma_f32_16x16x32_bf16 v[34:37], v[142:145], v[196:199], 0
	s_nop 0
	v_mfma_f32_16x16x32_bf16 v[34:37], v[138:141], v[200:203], v[34:37]
	v_mfma_f32_16x16x32_bf16 v[26:29], v[134:137], v[196:199], 0
	s_nop 0
	v_mfma_f32_16x16x32_bf16 v[26:29], v[130:133], v[200:203], v[26:29]
	v_mfma_f32_16x16x32_bf16 v[18:21], v[142:145], v[204:207], 0
	s_nop 0
	v_mfma_f32_16x16x32_bf16 v[18:21], v[138:141], v[208:211], v[18:21]
	v_mfma_f32_16x16x32_bf16 v[10:13], v[134:137], v[204:207], 0
	s_nop 0
	v_mfma_f32_16x16x32_bf16 v[10:13], v[130:133], v[208:211], v[10:13]
	v_mfma_f32_16x16x32_bf16 v[6:9], v[142:145], v[212:215], 0
	s_nop 0
	v_mfma_f32_16x16x32_bf16 v[6:9], v[138:141], v[216:219], v[6:9]
	v_mfma_f32_16x16x32_bf16 v[2:5], v[134:137], v[212:215], 0
	s_nop 0
	v_mfma_f32_16x16x32_bf16 v[2:5], v[130:133], v[216:219], v[2:5]
	s_setprio 0
	s_barrier
	v_add_u32_e32 v142, 0x18000, v186
	v_add_u32_e32 v158, 0x1c000, v186
	ds_read_b128 v[130:133], v142
	ds_read_b128 v[134:137], v142 offset:1024
	ds_read_b128 v[138:141], v142 offset:2048
	ds_read_b128 v[142:145], v142 offset:3072
	ds_read_b128 v[146:149], v158
	ds_read_b128 v[150:153], v158 offset:1024
	ds_read_b128 v[154:157], v158 offset:2048
	ds_read_b128 v[158:161], v158 offset:3072
	s_mov_b32 m0, s28
	ds_read_b128 v[188:191], v187 offset:32768
	ds_read_b128 v[192:195], v187 offset:33792
	ds_read_b128 v[196:199], v187 offset:34816
	ds_read_b128 v[200:203], v187 offset:35840
	ds_read_b128 v[204:207], v187 offset:36864
	ds_read_b128 v[208:211], v187 offset:37888
	ds_read_b128 v[212:215], v187 offset:38912
	ds_read_b128 v[216:219], v187 offset:39936
	buffer_load_dwordx4 v183, s[4:7], s57 offen lds
	s_mov_b32 m0, s29
	s_nop 0
	buffer_load_dwordx4 v184, s[4:7], s57 offen lds
	s_waitcnt vmcnt(8)
	s_waitcnt lgkmcnt(0)
	s_barrier
	s_setprio 1
	s_waitcnt lgkmcnt(7)
	v_mfma_f32_16x16x32_bf16 v[126:129], v[130:133], v[188:191], v[126:129]
	s_waitcnt lgkmcnt(6)
	v_mfma_f32_16x16x32_bf16 v[126:129], v[134:137], v[192:195], v[126:129]
	v_mfma_f32_16x16x32_bf16 v[122:125], v[138:141], v[188:191], v[122:125]
	s_nop 0
	v_mfma_f32_16x16x32_bf16 v[122:125], v[142:145], v[192:195], v[122:125]
	s_waitcnt lgkmcnt(5)
	v_mfma_f32_16x16x32_bf16 v[118:121], v[130:133], v[196:199], v[118:121]
	s_waitcnt lgkmcnt(4)
	v_mfma_f32_16x16x32_bf16 v[118:121], v[134:137], v[200:203], v[118:121]
	v_mfma_f32_16x16x32_bf16 v[110:113], v[138:141], v[196:199], v[110:113]
	s_nop 0
	v_mfma_f32_16x16x32_bf16 v[110:113], v[142:145], v[200:203], v[110:113]
	s_waitcnt lgkmcnt(3)
	v_mfma_f32_16x16x32_bf16 v[102:105], v[130:133], v[204:207], v[102:105]
	s_waitcnt lgkmcnt(2)
	v_mfma_f32_16x16x32_bf16 v[102:105], v[134:137], v[208:211], v[102:105]
	v_mfma_f32_16x16x32_bf16 v[94:97], v[138:141], v[204:207], v[94:97]
	s_nop 0
	v_mfma_f32_16x16x32_bf16 v[94:97], v[142:145], v[208:211], v[94:97]
	s_waitcnt lgkmcnt(1)
	v_mfma_f32_16x16x32_bf16 v[86:89], v[130:133], v[212:215], v[86:89]
	s_waitcnt lgkmcnt(0)
	v_mfma_f32_16x16x32_bf16 v[86:89], v[134:137], v[216:219], v[86:89]
	v_mfma_f32_16x16x32_bf16 v[78:81], v[138:141], v[212:215], v[78:81]
	s_nop 0
	v_mfma_f32_16x16x32_bf16 v[78:81], v[142:145], v[216:219], v[78:81]
	s_setprio 0
	s_setprio 1
	v_mfma_f32_16x16x32_bf16 v[114:117], v[146:149], v[188:191], v[114:117]
	s_nop 0
	v_mfma_f32_16x16x32_bf16 v[114:117], v[150:153], v[192:195], v[114:117]
	v_mfma_f32_16x16x32_bf16 v[106:109], v[154:157], v[188:191], v[106:109]
	s_nop 0
	v_mfma_f32_16x16x32_bf16 v[106:109], v[158:161], v[192:195], v[106:109]
	v_mfma_f32_16x16x32_bf16 v[98:101], v[146:149], v[196:199], v[98:101]
	s_nop 0
	v_mfma_f32_16x16x32_bf16 v[98:101], v[150:153], v[200:203], v[98:101]
	v_mfma_f32_16x16x32_bf16 v[90:93], v[154:157], v[196:199], v[90:93]
	s_nop 0
	v_mfma_f32_16x16x32_bf16 v[90:93], v[158:161], v[200:203], v[90:93]
	v_mfma_f32_16x16x32_bf16 v[82:85], v[146:149], v[204:207], v[82:85]
	s_nop 0
	v_mfma_f32_16x16x32_bf16 v[82:85], v[150:153], v[208:211], v[82:85]
	v_mfma_f32_16x16x32_bf16 v[74:77], v[154:157], v[204:207], v[74:77]
	s_nop 0
	v_mfma_f32_16x16x32_bf16 v[74:77], v[158:161], v[208:211], v[74:77]
	v_mfma_f32_16x16x32_bf16 v[70:73], v[146:149], v[212:215], v[70:73]
	s_nop 0
	v_mfma_f32_16x16x32_bf16 v[70:73], v[150:153], v[216:219], v[70:73]
	v_mfma_f32_16x16x32_bf16 v[66:69], v[154:157], v[212:215], v[66:69]
	s_nop 0
	v_mfma_f32_16x16x32_bf16 v[66:69], v[158:161], v[216:219], v[66:69]
	s_setprio 0
	s_barrier
; #define PG8_STAGE_A(bufoff, soff, voff) do { _Pragma("unroll") for (int _i = 0; _i < 2; ++_i) \
;         __builtin_amdgcn_raw_ptr_buffer_load_lds(rsA, (LAS void*)(lds + (bufoff) + ldsw + _i * 8192), 16, (voff)[_i], (soff), 0, 0); } while (0)
; #define PG8_STAGE_B(bufoff, soff) do { _Pragma("unroll") for (int _i = 0; _i < 2; ++_i) \
;         __builtin_amdgcn_raw_ptr_buffer_load_lds(rsB, (LAS void*)(lds + (bufoff) + ldsw + _i * 8192), 16, voffB[_i], (soff), 0, 0); } while (0)
; #define PG8_LDA(dst, b, h) do { _Pragma("unroll") for (int m = 0; m < 4; ++m) dst[m] = PG8_LD8(lds + PG8_SA(b, h) + aoff + m * 2048); } while (0)
; #define PG8_WAIT_V(n) asm volatile("s_waitcnt vmcnt(" #n ")" ::: "memory")
; #define PG8_WAIT_L(n) asm volatile("s_waitcnt lgkmcnt(" #n ")" ::: "memory")
; #define PG8_BAR __builtin_amdgcn_s_barrier()
; #define PG8_SCHED __builtin_amdgcn_sched_barrier(0)
; template <class Epi, class Sched, bool GATHER, bool ALIGN_EPI, bool SP2, bool FP8>
; __device__ __forceinline__ void gemm_phase(LAS unsigned char* lds, const Gemm g, const Sched& S, const Epi& E) {
;     ...
;         for (int t = 0; t < nt; t += 2) {
;     ...
;             PG8_WAIT_V(8); PG8_WAIT_L(0); PG8_BAR; PG8_MMA(0, 0, At, B0); PG8_MMA(0, 1, At, B1); PG8_BAR; PG8_SCHED;
;             PG8_LDA(At, 1, 1); PG8_STAGE_B(PG8_SB(1, 0), b3); PG8_STAGE_B(PG8_SB(1, 1), b3 + hstep); PG8_STAGE_A(PG8_SA(1, 0), a3, va20);
;             PG8_WAIT_V(8); PG8_WAIT_L(0); PG8_BAR; PG8_MMA(1, 0, At, B0); PG8_MMA(1, 1, At, B1); PG8_BAR; PG8_SCHED;
	s_mov_b32 m0, s31
	s_or_b32 s57, s56, 0x80
	ds_read_b128 v[188:191], v187 offset:49152
	ds_read_b128 v[192:195], v187 offset:50176
	ds_read_b128 v[196:199], v187 offset:51200
	ds_read_b128 v[200:203], v187 offset:52224
	ds_read_b128 v[204:207], v187 offset:53248
	ds_read_b128 v[208:211], v187 offset:54272
	ds_read_b128 v[212:215], v187 offset:55296
	ds_read_b128 v[216:219], v187 offset:56320
	buffer_load_dwordx4 v165, s[8:11], s57 offen lds
	s_mov_b32 m0, s34
	s_add_i32 s56, s56, 0x80080
	buffer_load_dwordx4 v180, s[8:11], s57 offen lds
	s_mov_b32 m0, s37
	s_nop 0
	buffer_load_dwordx4 v165, s[8:11], s56 offen lds
	s_mov_b32 m0, s38
	s_nop 0
	buffer_load_dwordx4 v180, s[8:11], s56 offen lds
	s_mov_b32 m0, s35
	s_nop 0
	buffer_load_dwordx4 v181, s[4:7], s53 offen lds
	s_mov_b32 m0, s36
	s_nop 0
	buffer_load_dwordx4 v182, s[4:7], s53 offen lds
	s_waitcnt vmcnt(8)
	s_waitcnt lgkmcnt(0)
	s_barrier
	s_setprio 1
	s_waitcnt lgkmcnt(7)
	v_mfma_f32_16x16x32_bf16 v[62:65], v[130:133], v[188:191], v[62:65]
	s_waitcnt lgkmcnt(6)
	v_mfma_f32_16x16x32_bf16 v[62:65], v[134:137], v[192:195], v[62:65]
	v_mfma_f32_16x16x32_bf16 v[58:61], v[138:141], v[188:191], v[58:61]
	s_nop 0
	v_mfma_f32_16x16x32_bf16 v[58:61], v[142:145], v[192:195], v[58:61]
	s_waitcnt lgkmcnt(5)
	v_mfma_f32_16x16x32_bf16 v[54:57], v[130:133], v[196:199], v[54:57]
	s_waitcnt lgkmcnt(4)
	v_mfma_f32_16x16x32_bf16 v[54:57], v[134:137], v[200:203], v[54:57]
	v_mfma_f32_16x16x32_bf16 v[46:49], v[138:141], v[196:199], v[46:49]
	s_nop 0
	v_mfma_f32_16x16x32_bf16 v[46:49], v[142:145], v[200:203], v[46:49]
	s_waitcnt lgkmcnt(3)
	v_mfma_f32_16x16x32_bf16 v[38:41], v[130:133], v[204:207], v[38:41]
	s_waitcnt lgkmcnt(2)
	v_mfma_f32_16x16x32_bf16 v[38:41], v[134:137], v[208:211], v[38:41]
	v_mfma_f32_16x16x32_bf16 v[30:33], v[138:141], v[204:207], v[30:33]
	s_nop 0
	v_mfma_f32_16x16x32_bf16 v[30:33], v[142:145], v[208:211], v[30:33]
	s_waitcnt lgkmcnt(1)
	v_mfma_f32_16x16x32_bf16 v[22:25], v[130:133], v[212:215], v[22:25]
	s_waitcnt lgkmcnt(0)
	v_mfma_f32_16x16x32_bf16 v[22:25], v[134:137], v[216:219], v[22:25]
	v_mfma_f32_16x16x32_bf16 v[14:17], v[138:141], v[212:215], v[14:17]
	s_nop 0
	v_mfma_f32_16x16x32_bf16 v[14:17], v[142:145], v[216:219], v[14:17]
	s_setprio 0
	s_setprio 1
	v_mfma_f32_16x16x32_bf16 v[50:53], v[146:149], v[188:191], v[50:53]
	s_nop 0
	v_mfma_f32_16x16x32_bf16 v[50:53], v[150:153], v[192:195], v[50:53]
	v_mfma_f32_16x16x32_bf16 v[42:45], v[154:157], v[188:191], v[42:45]
	s_nop 0
	v_mfma_f32_16x16x32_bf16 v[42:45], v[158:161], v[192:195], v[42:45]
	v_mfma_f32_16x16x32_bf16 v[34:37], v[146:149], v[196:199], v[34:37]
	s_nop 0
	v_mfma_f32_16x16x32_bf16 v[34:37], v[150:153], v[200:203], v[34:37]
	v_mfma_f32_16x16x32_bf16 v[26:29], v[154:157], v[196:199], v[26:29]
	s_nop 0
	v_mfma_f32_16x16x32_bf16 v[26:29], v[158:161], v[200:203], v[26:29]
	v_mfma_f32_16x16x32_bf16 v[18:21], v[146:149], v[204:207], v[18:21]
	s_nop 0
	v_mfma_f32_16x16x32_bf16 v[18:21], v[150:153], v[208:211], v[18:21]
	v_mfma_f32_16x16x32_bf16 v[10:13], v[154:157], v[204:207], v[10:13]
	s_nop 0
	v_mfma_f32_16x16x32_bf16 v[10:13], v[158:161], v[208:211], v[10:13]
	v_mfma_f32_16x16x32_bf16 v[6:9], v[146:149], v[212:215], v[6:9]
	s_nop 0
	v_mfma_f32_16x16x32_bf16 v[6:9], v[150:153], v[216:219], v[6:9]
	v_mfma_f32_16x16x32_bf16 v[2:5], v[154:157], v[212:215], v[2:5]
	s_nop 0
	v_mfma_f32_16x16x32_bf16 v[2:5], v[158:161], v[216:219], v[2:5]
	s_setprio 0
	s_barrier
	s_add_i32 s52, s52, 2
	s_addk_i32 s50, 0x100
	s_addk_i32 s51, 0x100
	s_branch .LBB0_192

; #define PG8_SETA(d0, d1, u) do { d0.x = PG8_OFFA(u, Rr[0], 0); d0.y = PG8_OFFA(u, Rr[1], 1); d1.x = PG8_OFFA(u, HALF + Rr[0], 0); d1.y = PG8_OFFA(u, HALF + Rr[1], 1); } while (0)
; #define PG8_STAGE_A(bufoff, soff, voff) do { _Pragma("unroll") for (int _i = 0; _i < 2; ++_i) \
;         __builtin_amdgcn_raw_ptr_buffer_load_lds(rsA, (LAS void*)(lds + (bufoff) + ldsw + _i * 8192), 16, (voff)[_i], (soff), 0, 0); } while (0)
; #define PG8_STAGE_B(bufoff, soff) do { _Pragma("unroll") for (int _i = 0; _i < 2; ++_i) \
;         __builtin_amdgcn_raw_ptr_buffer_load_lds(rsB, (LAS void*)(lds + (bufoff) + ldsw + _i * 8192), 16, voffB[_i], (soff), 0, 0); } while (0)
; #define PG8_LDA(dst, b, h) do { _Pragma("unroll") for (int m = 0; m < 4; ++m) dst[m] = PG8_LD8(lds + PG8_SA(b, h) + aoff + m * 2048); } while (0)
; #define PG8_WAIT_V(n) asm volatile("s_waitcnt vmcnt(" #n ")" ::: "memory")
; template <class Epi, class Sched, bool GATHER, bool ALIGN_EPI, bool SP2, bool FP8>
; __device__ __forceinline__ void gemm_phase(LAS unsigned char* lds, const Gemm g, const Sched& S, const Epi& E) {
;     ...
;     for (;;) {
;         const bool has_next = S.next(ui + 1, nxt);
;         const int nA = has_next ? (GATHER ? 0 : nxt.pm * tstep) : cA, nB = has_next ? nxt.pn * tstep : cB;
;         u32x2 nvA0 = vA0, nvA1 = vA1;
;         if constexpr (GATHER) { if (has_next) PG8_SETA(nvA0, nvA1, nxt); }
;         for (int t = 0; t < nt; t += 2) {
;             const bool last = (t == nt - 2);
;             if (last) pre = E.prefetch(cur, wr, wc, fr, fq);
;             const int a1 = cA + (t + 1) * kstep;
;             const int a2 = last ? nA : cA + (t + 2) * kstep, b2 = last ? nB : cB + (t + 2) * kstep;
;             const int a3 = a2 + kstep, b3 = b2 + kstep;
;             const u32x2 va20 = (GATHER && last) ? nvA0 : vA0, va21 = (GATHER && last) ? nvA1 : vA1;
;             if constexpr (SP2) {
;             PG8_LDB(B0, 0, 0); PG8_LDB(B1, 0, 1); PG8_SCHED; PG8_LDA(At, 0, 0); PG8_STAGE_A(PG8_SA(1, 1), a1, vA1);
;             PG8_WAIT_V(8); PG8_WAIT_L(0); PG8_BAR; PG8_MMA(0, 0, At, B0); PG8_MMA(0, 1, At, B1); PG8_BAR; PG8_SCHED;
;             PG8_LDA(At, 0, 1); PG8_STAGE_B(PG8_SB(0, 0), b2); PG8_STAGE_B(PG8_SB(0, 1), b2 + hstep); PG8_STAGE_A(PG8_SA(0, 0), a2, va20);
;             PG8_WAIT_V(8); PG8_WAIT_L(0); PG8_BAR; PG8_MMA(1, 0, At, B0); PG8_MMA(1, 1, At, B1); PG8_BAR; PG8_SCHED;
.LBB0_1004:
	s_lshl_b32 s63, s59, 19
	s_and_b64 s[10:11], s[0:1], exec
	s_cselect_b32 s33, s63, s69
	s_lshl_b32 s64, s60, 19
	s_and_b64 s[10:11], s[0:1], exec
	s_cselect_b32 s68, s64, s70
	s_lshl_b32 s10, s66, 11
	s_lshl_b32 s11, s65, 8
	s_sub_i32 s11, s11, s10
	v_readlane_b32 s80, v245, 8
	v_or_b32_e32 v2, s11, v174
	s_ashr_i32 s11, s10, 31
	v_readlane_b32 s86, v245, 14
	v_readlane_b32 s87, v245, 15
	s_lshl_b64 s[10:11], s[10:11], 2
	s_mov_b64 s[74:75], s[86:87]
	v_readlane_b32 s82, v245, 10
	v_readlane_b32 s83, v245, 11
	s_add_u32 s10, s74, s10
	s_addc_u32 s11, s75, s11
	v_ashrrev_i32_e32 v3, 31, v2
	v_readlane_b32 s82, v244, 0
	v_lshl_add_u64 v[166:167], v[2:3], 2, s[10:11]
	s_addk_i32 s69, 0x80
	s_addk_i32 s70, 0x100
	s_mov_b32 s71, -2
	v_readlane_b32 s83, v244, 1
	v_readlane_b32 s81, v245, 9
	v_readlane_b32 s84, v245, 12
	v_readlane_b32 s85, v245, 13
	s_mov_b64 s[10:11], 0
	s_add_i32 s74, s69, 0x80
	s_and_b64 s[72:73], s[10:11], exec
	s_cselect_b32 s74, s33, s74
	s_or_b32 s73, s74, 0x80
	s_and_b64 s[10:11], s[10:11], exec
	s_cselect_b32 s72, s68, s70
	s_mov_b32 s10, s6
	s_mov_b32 s11, s7
	v_add_u32_e32 v14, 0x10000, v175
	ds_read_b128 v[2:5], v14
	ds_read_b128 v[6:9], v14 offset:1024
	ds_read_b128 v[10:13], v14 offset:2048
	ds_read_b128 v[14:17], v14 offset:3072
	v_add_u32_e32 v177, 0x14000, v175
	ds_read_b128 v[210:213], v177
	ds_read_b128 v[214:217], v177 offset:1024
	ds_read_b128 v[218:221], v177 offset:2048
	ds_read_b128 v[222:225], v177 offset:3072
	ds_read_b128 v[178:181], v176
	ds_read_b128 v[182:185], v176 offset:1024
	ds_read_b128 v[186:189], v176 offset:2048
	ds_read_b128 v[190:193], v176 offset:3072
	ds_read_b128 v[194:197], v176 offset:4096
	ds_read_b128 v[198:201], v176 offset:5120
	ds_read_b128 v[202:205], v176 offset:6144
	ds_read_b128 v[206:209], v176 offset:7168
	s_mov_b32 m0, s36
	s_nop 0
	buffer_load_dwordx4 v172, s[4:7], s69 offen lds
	s_mov_b32 m0, s37
	s_nop 0
	buffer_load_dwordx4 v173, s[4:7], s69 offen lds
	s_waitcnt vmcnt(8)
	s_waitcnt lgkmcnt(0)
	s_barrier
	s_setprio 1
	v_mfma_f32_16x16x128_f8f6f4 v[158:161], v[2:9], v[178:185], 0
	v_mfma_f32_16x16x128_f8f6f4 v[154:157], v[10:17], v[178:185], 0
	v_mfma_f32_16x16x128_f8f6f4 v[142:145], v[2:9], v[186:193], 0
	v_mfma_f32_16x16x128_f8f6f4 v[138:141], v[10:17], v[186:193], 0
	v_mfma_f32_16x16x128_f8f6f4 v[126:129], v[2:9], v[194:201], 0
	v_mfma_f32_16x16x128_f8f6f4 v[122:125], v[10:17], v[194:201], 0
	v_mfma_f32_16x16x128_f8f6f4 v[110:113], v[2:9], v[202:209], 0
	v_mfma_f32_16x16x128_f8f6f4 v[106:109], v[10:17], v[202:209], 0
	v_mfma_f32_16x16x128_f8f6f4 v[150:153], v[210:217], v[178:185], 0
	v_mfma_f32_16x16x128_f8f6f4 v[146:149], v[218:225], v[178:185], 0
	v_mfma_f32_16x16x128_f8f6f4 v[134:137], v[210:217], v[186:193], 0
	v_mfma_f32_16x16x128_f8f6f4 v[130:133], v[218:225], v[186:193], 0
	v_mfma_f32_16x16x128_f8f6f4 v[118:121], v[210:217], v[194:201], 0
	v_mfma_f32_16x16x128_f8f6f4 v[114:117], v[218:225], v[194:201], 0
	v_mfma_f32_16x16x128_f8f6f4 v[102:105], v[210:217], v[202:209], 0
	v_mfma_f32_16x16x128_f8f6f4 v[98:101], v[218:225], v[202:209], 0
	s_setprio 0
	s_barrier
	ds_read_b128 v[178:181], v176 offset:16384
	ds_read_b128 v[182:185], v176 offset:17408
	ds_read_b128 v[186:189], v176 offset:18432
	ds_read_b128 v[190:193], v176 offset:19456
	ds_read_b128 v[194:197], v176 offset:20480
	ds_read_b128 v[198:201], v176 offset:21504
	ds_read_b128 v[202:205], v176 offset:22528
	ds_read_b128 v[206:209], v176 offset:23552
	s_mov_b32 m0, s21
	s_nop 0
	buffer_load_dwordx4 v163, s[8:11], s72 offen lds
	s_mov_b32 m0, s22
	s_nop 0
	buffer_load_dwordx4 v168, s[8:11], s72 offen lds
	s_add_i32 s75, s72, 0x40000
	s_mov_b32 m0, s24
	s_nop 0
	buffer_load_dwordx4 v163, s[8:11], s75 offen lds
	s_mov_b32 m0, s25
	s_nop 0
	buffer_load_dwordx4 v168, s[8:11], s75 offen lds
	s_mov_b32 m0, s20
	s_nop 0
	buffer_load_dwordx4 v170, s[4:7], s74 offen lds
	s_mov_b32 m0, s23
	s_nop 0
	buffer_load_dwordx4 v171, s[4:7], s74 offen lds
	s_waitcnt vmcnt(8)
	s_waitcnt lgkmcnt(0)
	s_barrier
	s_setprio 1
	v_mfma_f32_16x16x128_f8f6f4 v[94:97], v[2:9], v[178:185], 0
	v_mfma_f32_16x16x128_f8f6f4 v[90:93], v[10:17], v[178:185], 0
	v_mfma_f32_16x16x128_f8f6f4 v[78:81], v[2:9], v[186:193], 0
	v_mfma_f32_16x16x128_f8f6f4 v[74:77], v[10:17], v[186:193], 0
	v_mfma_f32_16x16x128_f8f6f4 v[62:65], v[2:9], v[194:201], 0
	v_mfma_f32_16x16x128_f8f6f4 v[58:61], v[10:17], v[194:201], 0
	v_mfma_f32_16x16x128_f8f6f4 v[46:49], v[2:9], v[202:209], 0
	v_mfma_f32_16x16x128_f8f6f4 v[42:45], v[10:17], v[202:209], 0
	v_mfma_f32_16x16x128_f8f6f4 v[86:89], v[210:217], v[178:185], 0
	v_mfma_f32_16x16x128_f8f6f4 v[82:85], v[218:225], v[178:185], 0
	v_mfma_f32_16x16x128_f8f6f4 v[70:73], v[210:217], v[186:193], 0
	v_mfma_f32_16x16x128_f8f6f4 v[66:69], v[218:225], v[186:193], 0
	v_mfma_f32_16x16x128_f8f6f4 v[54:57], v[210:217], v[194:201], 0
	v_mfma_f32_16x16x128_f8f6f4 v[50:53], v[218:225], v[194:201], 0
	v_mfma_f32_16x16x128_f8f6f4 v[38:41], v[210:217], v[202:209], 0
	v_mfma_f32_16x16x128_f8f6f4 v[34:37], v[218:225], v[202:209], 0
	s_setprio 0
	s_barrier
; #define PG8_STAGE_A(bufoff, soff, voff) do { _Pragma("unroll") for (int _i = 0; _i < 2; ++_i) \
;         __builtin_amdgcn_raw_ptr_buffer_load_lds(rsA, (LAS void*)(lds + (bufoff) + ldsw + _i * 8192), 16, (voff)[_i], (soff), 0, 0); } while (0)
; #define PG8_STAGE_B(bufoff, soff) do { _Pragma("unroll") for (int _i = 0; _i < 2; ++_i) \
;         __builtin_amdgcn_raw_ptr_buffer_load_lds(rsB, (LAS void*)(lds + (bufoff) + ldsw + _i * 8192), 16, voffB[_i], (soff), 0, 0); } while (0)
; #define PG8_LDA(dst, b, h) do { _Pragma("unroll") for (int m = 0; m < 4; ++m) dst[m] = PG8_LD8(lds + PG8_SA(b, h) + aoff + m * 2048); } while (0)
; #define PG8_LDB(dst, b, h) do { _Pragma("unroll") for (int n = 0; n < 2; ++n) dst[n] = PG8_LD8(lds + PG8_SB(b, h) + boff + n * 2048); } while (0)
; #define PG8_WAIT_V(n) asm volatile("s_waitcnt vmcnt(" #n ")" ::: "memory")
; #define PG8_WAIT_L(n) asm volatile("s_waitcnt lgkmcnt(" #n ")" ::: "memory")
; #define PG8_BAR __builtin_amdgcn_s_barrier()
; #define PG8_SCHED __builtin_amdgcn_sched_barrier(0)
; template <class Epi, class Sched, bool GATHER, bool ALIGN_EPI, bool SP2, bool FP8>
; __device__ __forceinline__ void gemm_phase(LAS unsigned char* lds, const Gemm g, const Sched& S, const Epi& E) {
;     ...
;             PG8_LDB(B0, 1, 0); PG8_LDB(B1, 1, 1); PG8_SCHED; PG8_LDA(At, 1, 0); PG8_STAGE_A(PG8_SA(0, 1), a2, va21);
;             PG8_WAIT_V(8); PG8_WAIT_L(0); PG8_BAR; PG8_MMA(0, 0, At, B0); PG8_MMA(0, 1, At, B1); PG8_BAR; PG8_SCHED;
;             PG8_LDA(At, 1, 1); PG8_STAGE_B(PG8_SB(1, 0), b3); PG8_STAGE_B(PG8_SB(1, 1), b3 + hstep); PG8_STAGE_A(PG8_SA(1, 0), a3, va20);
;             PG8_WAIT_V(8); PG8_WAIT_L(0); PG8_BAR; PG8_MMA(1, 0, At, B0); PG8_MMA(1, 1, At, B1); PG8_BAR; PG8_SCHED;
	v_add_u32_e32 v14, 0x18000, v175
	ds_read_b128 v[2:5], v14
	ds_read_b128 v[6:9], v14 offset:1024
	ds_read_b128 v[10:13], v14 offset:2048
	ds_read_b128 v[14:17], v14 offset:3072
	v_add_u32_e32 v177, 0x1c000, v175
	ds_read_b128 v[210:213], v177
	ds_read_b128 v[214:217], v177 offset:1024
	ds_read_b128 v[218:221], v177 offset:2048
	ds_read_b128 v[222:225], v177 offset:3072
	ds_read_b128 v[178:181], v176 offset:32768
	ds_read_b128 v[182:185], v176 offset:33792
	ds_read_b128 v[186:189], v176 offset:34816
	ds_read_b128 v[190:193], v176 offset:35840
	ds_read_b128 v[194:197], v176 offset:36864
	ds_read_b128 v[198:201], v176 offset:37888
	ds_read_b128 v[202:205], v176 offset:38912
	ds_read_b128 v[206:209], v176 offset:39936
	s_mov_b32 m0, s26
	s_nop 0
	buffer_load_dwordx4 v172, s[4:7], s74 offen lds
	s_mov_b32 m0, s27
	s_nop 0
	buffer_load_dwordx4 v173, s[4:7], s74 offen lds
	s_waitcnt vmcnt(8)
	s_waitcnt lgkmcnt(0)
	s_barrier
	s_setprio 1
	v_mfma_f32_16x16x128_f8f6f4 v[158:161], v[2:9], v[178:185], v[158:161]
	v_mfma_f32_16x16x128_f8f6f4 v[154:157], v[10:17], v[178:185], v[154:157]
	v_mfma_f32_16x16x128_f8f6f4 v[142:145], v[2:9], v[186:193], v[142:145]
	v_mfma_f32_16x16x128_f8f6f4 v[138:141], v[10:17], v[186:193], v[138:141]
	v_mfma_f32_16x16x128_f8f6f4 v[126:129], v[2:9], v[194:201], v[126:129]
	v_mfma_f32_16x16x128_f8f6f4 v[122:125], v[10:17], v[194:201], v[122:125]
	v_mfma_f32_16x16x128_f8f6f4 v[110:113], v[2:9], v[202:209], v[110:113]
	v_mfma_f32_16x16x128_f8f6f4 v[106:109], v[10:17], v[202:209], v[106:109]
	v_mfma_f32_16x16x128_f8f6f4 v[150:153], v[210:217], v[178:185], v[150:153]
	v_mfma_f32_16x16x128_f8f6f4 v[146:149], v[218:225], v[178:185], v[146:149]
	v_mfma_f32_16x16x128_f8f6f4 v[134:137], v[210:217], v[186:193], v[134:137]
	v_mfma_f32_16x16x128_f8f6f4 v[130:133], v[218:225], v[186:193], v[130:133]
	v_mfma_f32_16x16x128_f8f6f4 v[118:121], v[210:217], v[194:201], v[118:121]
	v_mfma_f32_16x16x128_f8f6f4 v[114:117], v[218:225], v[194:201], v[114:117]
	v_mfma_f32_16x16x128_f8f6f4 v[102:105], v[210:217], v[202:209], v[102:105]
	v_mfma_f32_16x16x128_f8f6f4 v[98:101], v[218:225], v[202:209], v[98:101]
	s_setprio 0
	s_barrier
	ds_read_b128 v[178:181], v176 offset:49152
	ds_read_b128 v[182:185], v176 offset:50176
	ds_read_b128 v[186:189], v176 offset:51200
	ds_read_b128 v[190:193], v176 offset:52224
	ds_read_b128 v[194:197], v176 offset:53248
	ds_read_b128 v[198:201], v176 offset:54272
	ds_read_b128 v[202:205], v176 offset:55296
	ds_read_b128 v[206:209], v176 offset:56320
	s_or_b32 s72, s72, 0x80
	s_mov_b32 m0, s28
	s_nop 0
	buffer_load_dwordx4 v163, s[8:11], s72 offen lds
	s_mov_b32 m0, s29
	s_nop 0
	buffer_load_dwordx4 v168, s[8:11], s72 offen lds
	s_add_i32 s75, s72, 0x40000
	s_mov_b32 m0, s34
	s_nop 0
	buffer_load_dwordx4 v163, s[8:11], s75 offen lds
	s_mov_b32 m0, s35
	s_nop 0
	buffer_load_dwordx4 v168, s[8:11], s75 offen lds
	s_mov_b32 m0, s30
	s_nop 0
	buffer_load_dwordx4 v170, s[4:7], s73 offen lds
	s_mov_b32 m0, s31
	s_nop 0
	buffer_load_dwordx4 v171, s[4:7], s73 offen lds
	s_waitcnt vmcnt(8)
	s_waitcnt lgkmcnt(0)
	s_barrier
	s_setprio 1
	v_mfma_f32_16x16x128_f8f6f4 v[94:97], v[2:9], v[178:185], v[94:97]
	v_mfma_f32_16x16x128_f8f6f4 v[90:93], v[10:17], v[178:185], v[90:93]
	v_mfma_f32_16x16x128_f8f6f4 v[78:81], v[2:9], v[186:193], v[78:81]
	v_mfma_f32_16x16x128_f8f6f4 v[74:77], v[10:17], v[186:193], v[74:77]
	v_mfma_f32_16x16x128_f8f6f4 v[62:65], v[2:9], v[194:201], v[62:65]
	v_mfma_f32_16x16x128_f8f6f4 v[58:61], v[10:17], v[194:201], v[58:61]
	v_mfma_f32_16x16x128_f8f6f4 v[46:49], v[2:9], v[202:209], v[46:49]
	v_mfma_f32_16x16x128_f8f6f4 v[42:45], v[10:17], v[202:209], v[42:45]
	v_mfma_f32_16x16x128_f8f6f4 v[86:89], v[210:217], v[178:185], v[86:89]
	v_mfma_f32_16x16x128_f8f6f4 v[82:85], v[218:225], v[178:185], v[82:85]
	v_mfma_f32_16x16x128_f8f6f4 v[70:73], v[210:217], v[186:193], v[70:73]
	v_mfma_f32_16x16x128_f8f6f4 v[66:69], v[218:225], v[186:193], v[66:69]
	v_mfma_f32_16x16x128_f8f6f4 v[54:57], v[210:217], v[194:201], v[54:57]
	v_mfma_f32_16x16x128_f8f6f4 v[50:53], v[218:225], v[194:201], v[50:53]
	v_mfma_f32_16x16x128_f8f6f4 v[38:41], v[210:217], v[202:209], v[38:41]
	v_mfma_f32_16x16x128_f8f6f4 v[34:37], v[218:225], v[202:209], v[34:37]
	s_setprio 0
	s_add_i32 s71, s71, 2
	s_addk_i32 s69, 0x100
	s_addk_i32 s70, 0x100
	s_barrier
	s_branch .LBB0_1006
